# speedup vs baseline: 1.0080x; 1.0031x over previous
_Z15qkv_proj_kernelPKDF16_S0_PKfS2_S2_PDF16_S3_S3_:
	s_lshr_b32 s4, s2, 2
	s_and_b32 s3, s2, 7
	s_and_b32 s22, s4, 8
	s_or_b32 s4, s22, s3
	v_readfirstlane_b32 s18, v0
	s_ashr_i32 s3, s2, 6
	s_lshl_b32 s21, s4, 8
	s_bfe_u32 s20, s2, 0x20003
	v_and_b32_e32 v1, 63, v0
	s_cmpk_lt_u32 s18, 0x200
	s_mulk_i32 s20, 0xc0
	s_cbranch_scc1 .LBB1_30
	s_setprio 2
	s_load_dwordx4 s[4:7], s[0:1], 0x0
	s_sub_i32 s10, 2, s3
	s_lshr_b32 s12, s18, 6
	s_add_i32 s12, s12, -8
	s_mul_i32 s13, s10, 0x600000
	s_mul_hi_i32 s14, s10, 0x600000
	s_mul_i32 s15, s10, 0x120000
	s_waitcnt lgkmcnt(0)
	s_add_u32 s4, s4, s13
	s_addc_u32 s5, s5, s14
	s_add_u32 s6, s6, s15
	s_addc_u32 s7, s7, 0
	v_lshrrev_b32_e32 v2, 2, v1
	v_lshrrev_b32_e32 v3, 4, v1
	v_xor_b32_e32 v3, v3, v1
	v_and_b32_e32 v3, 3, v3
	v_lshlrev_b32_e32 v3, 4, v3
	v_mul_u32_u24_e32 v2, 0x600, v2
	v_add_u32_e32 v2, v2, v3
	s_mul_i32 s16, s12, 7
	s_mul_i32 s27, s20, 0x600
	s_add_u32 s6, s6, s27
	s_addc_u32 s7, s7, 0
	s_add_i32 s27, s21, -192
	s_mul_i32 s27, s27, 0x600
	s_ashr_i32 s28, s27, 31
	s_add_u32 s4, s4, s27
	s_addc_u32 s5, s5, s28
	s_add_i32 s17, s16, 0
	s_cmp_ge_u32 s17, 12
	s_cselect_b32 s24, s4, s6
	s_cselect_b32 s25, s5, s7
	s_mul_i32 s17, s17, 0x6000
	s_add_u32 s30, s24, s17
	s_addc_u32 s31, s25, 0
	s_add_i32 s17, s16, 1
	s_cmp_ge_u32 s17, 12
	s_cselect_b32 s24, s4, s6
	s_cselect_b32 s25, s5, s7
	s_mul_i32 s17, s17, 0x6000
	s_add_i32 s17, s17, -1024
	s_add_u32 s32, s24, s17
	s_addc_u32 s33, s25, 0
	s_add_i32 s17, s16, 2
	s_cmp_ge_u32 s17, 12
	s_cselect_b32 s24, s4, s6
	s_cselect_b32 s25, s5, s7
	s_mul_i32 s17, s17, 0x6000
	s_add_i32 s17, s17, -2048
	s_add_u32 s34, s24, s17
	s_addc_u32 s35, s25, 0
	s_add_i32 s17, s16, 3
	s_cmp_ge_u32 s17, 12
	s_cselect_b32 s24, s4, s6
	s_cselect_b32 s25, s5, s7
	s_mul_i32 s17, s17, 0x6000
	s_add_u32 s36, s24, s17
	s_addc_u32 s37, s25, 0
	s_add_i32 s17, s16, 4
	s_cmp_ge_u32 s17, 12
	s_cselect_b32 s24, s4, s6
	s_cselect_b32 s25, s5, s7
	s_mul_i32 s17, s17, 0x6000
	s_add_i32 s17, s17, -1024
	s_add_u32 s38, s24, s17
	s_addc_u32 s39, s25, 0
	s_add_i32 s17, s16, 5
	s_cmp_ge_u32 s17, 12
	s_cselect_b32 s24, s4, s6
	s_cselect_b32 s25, s5, s7
	s_mul_i32 s17, s17, 0x6000
	s_add_i32 s17, s17, -2048
	s_add_u32 s40, s24, s17
	s_addc_u32 s41, s25, 0
	s_add_i32 s17, s16, 6
	s_cmp_ge_u32 s17, 12
	s_cselect_b32 s24, s4, s6
	s_cselect_b32 s25, s5, s7
	s_mul_i32 s17, s17, 0x6000
	s_add_u32 s42, s24, s17
	s_addc_u32 s43, s25, 0
	s_mul_i32 s26, s12, 0x1c00
	s_lshl_b32 s11, s10, 3
	s_add_i32 s11, s11, 0x10
	s_load_dwordx2 s[8:9], s[0:1], s11
	s_cmp_eq_u32 s10, 0
	s_cselect_b32 s29, 0x3e38aa3b, 1.0
	v_lshl_add_u32 v19, s12, 6, v1
	v_lshlrev_b32_e32 v21, 2, v19
	v_add_u32_e32 v21, 0x23800, v21
	v_min_u32_e32 v19, 0xbf, v19
	v_add_u32_e32 v19, s20, v19
	v_lshlrev_b32_e32 v19, 2, v19
	s_waitcnt lgkmcnt(0)
	global_load_dword v20, v19, s[8:9]
	s_add_i32 m0, s26, 2048
	s_nop 0
	global_load_lds_dwordx4 v2, s[30:31]
	global_load_lds_dwordx4 v2, s[32:33] offset:1024
	global_load_lds_dwordx4 v2, s[34:35] offset:2048
	s_add_i32 m0, s26, 5120
	s_nop 0
	global_load_lds_dwordx4 v2, s[36:37]
	global_load_lds_dwordx4 v2, s[38:39] offset:1024
	global_load_lds_dwordx4 v2, s[40:41] offset:2048
	s_add_i32 m0, s26, 8192
	s_nop 0
	global_load_lds_dwordx4 v2, s[42:43]
	s_add_i32 m0, s26, 30656
	s_nop 0
	global_load_lds_dwordx4 v2, s[30:31] offset:64
	global_load_lds_dwordx4 v2, s[32:33] offset:1088
	global_load_lds_dwordx4 v2, s[34:35] offset:2112
	s_add_i32 m0, s26, 33728
	s_nop 0
	global_load_lds_dwordx4 v2, s[36:37] offset:64
	global_load_lds_dwordx4 v2, s[38:39] offset:1088
	global_load_lds_dwordx4 v2, s[40:41] offset:2112
	s_add_i32 m0, s26, 36800
	s_nop 0
	global_load_lds_dwordx4 v2, s[42:43] offset:64
	s_add_i32 m0, s26, 59264
	s_nop 0
	global_load_lds_dwordx4 v2, s[30:31] offset:128
	global_load_lds_dwordx4 v2, s[32:33] offset:1152
	global_load_lds_dwordx4 v2, s[34:35] offset:2176
	s_add_i32 m0, s26, 62336
	s_nop 0
	global_load_lds_dwordx4 v2, s[36:37] offset:128
	global_load_lds_dwordx4 v2, s[38:39] offset:1152
	global_load_lds_dwordx4 v2, s[40:41] offset:2176
	s_add_i32 m0, s26, 65408
	s_nop 0
	global_load_lds_dwordx4 v2, s[42:43] offset:128
	s_add_i32 m0, s26, 87872
	s_nop 0
	global_load_lds_dwordx4 v2, s[30:31] offset:192
	global_load_lds_dwordx4 v2, s[32:33] offset:1216
	global_load_lds_dwordx4 v2, s[34:35] offset:2240
	s_add_i32 m0, s26, 90944
	s_nop 0
	global_load_lds_dwordx4 v2, s[36:37] offset:192
	global_load_lds_dwordx4 v2, s[38:39] offset:1216
	global_load_lds_dwordx4 v2, s[40:41] offset:2240
	s_add_i32 m0, s26, 94016
	s_nop 0
	global_load_lds_dwordx4 v2, s[42:43] offset:192
	s_waitcnt vmcnt(21)
	v_mul_f32_e32 v20, s29, v20
	ds_write_b32 v21, v20
	s_waitcnt lgkmcnt(0)
	s_barrier
	s_add_i32 m0, s26, 116480
	s_nop 0
	global_load_lds_dwordx4 v2, s[30:31] offset:256
	global_load_lds_dwordx4 v2, s[32:33] offset:1280
	global_load_lds_dwordx4 v2, s[34:35] offset:2304
	s_add_i32 m0, s26, 119552
	s_nop 0
	global_load_lds_dwordx4 v2, s[36:37] offset:256
	global_load_lds_dwordx4 v2, s[38:39] offset:1280
	global_load_lds_dwordx4 v2, s[40:41] offset:2304
	s_add_i32 m0, s26, 122624
	s_nop 0
	global_load_lds_dwordx4 v2, s[42:43] offset:256
	s_waitcnt vmcnt(21)
	s_barrier
	s_add_i32 m0, s26, 1728
	s_nop 0
	global_load_lds_dwordx4 v2, s[30:31] offset:320
	global_load_lds_dwordx4 v2, s[32:33] offset:1344
	global_load_lds_dwordx4 v2, s[34:35] offset:2368
	s_add_i32 m0, s26, 4800
	s_nop 0
	global_load_lds_dwordx4 v2, s[36:37] offset:320
	global_load_lds_dwordx4 v2, s[38:39] offset:1344
	global_load_lds_dwordx4 v2, s[40:41] offset:2368
	s_add_i32 m0, s26, 7872
	s_nop 0
	global_load_lds_dwordx4 v2, s[42:43] offset:320
	s_waitcnt vmcnt(21)
	s_barrier
	s_add_i32 m0, s26, 30336
	s_nop 0
	global_load_lds_dwordx4 v2, s[30:31] offset:384
	global_load_lds_dwordx4 v2, s[32:33] offset:1408
	global_load_lds_dwordx4 v2, s[34:35] offset:2432
	s_add_i32 m0, s26, 33408
	s_nop 0
	global_load_lds_dwordx4 v2, s[36:37] offset:384
	global_load_lds_dwordx4 v2, s[38:39] offset:1408
	global_load_lds_dwordx4 v2, s[40:41] offset:2432
	s_add_i32 m0, s26, 36480
	s_nop 0
	global_load_lds_dwordx4 v2, s[42:43] offset:384
	s_waitcnt vmcnt(21)
	s_barrier
	s_add_i32 m0, s26, 58944
	s_nop 0
	global_load_lds_dwordx4 v2, s[30:31] offset:448
	global_load_lds_dwordx4 v2, s[32:33] offset:1472
	global_load_lds_dwordx4 v2, s[34:35] offset:2496
	s_add_i32 m0, s26, 62016
	s_nop 0
	global_load_lds_dwordx4 v2, s[36:37] offset:448
	global_load_lds_dwordx4 v2, s[38:39] offset:1472
	global_load_lds_dwordx4 v2, s[40:41] offset:2496
	s_add_i32 m0, s26, 65088
	s_nop 0
	global_load_lds_dwordx4 v2, s[42:43] offset:448
	s_waitcnt vmcnt(21)
	s_barrier
	s_add_i32 m0, s26, 87552
	s_nop 0
	global_load_lds_dwordx4 v2, s[30:31] offset:512
	global_load_lds_dwordx4 v2, s[32:33] offset:1536
	global_load_lds_dwordx4 v2, s[34:35] offset:2560
	s_add_i32 m0, s26, 90624
	s_nop 0
	global_load_lds_dwordx4 v2, s[36:37] offset:512
	global_load_lds_dwordx4 v2, s[38:39] offset:1536
	global_load_lds_dwordx4 v2, s[40:41] offset:2560
	s_add_i32 m0, s26, 93696
	s_nop 0
	global_load_lds_dwordx4 v2, s[42:43] offset:512
	s_waitcnt vmcnt(21)
	s_barrier
	s_add_i32 m0, s26, 116160
	s_nop 0
	global_load_lds_dwordx4 v2, s[30:31] offset:576
	global_load_lds_dwordx4 v2, s[32:33] offset:1600
	global_load_lds_dwordx4 v2, s[34:35] offset:2624
	s_add_i32 m0, s26, 119232
	s_nop 0
	global_load_lds_dwordx4 v2, s[36:37] offset:576
	global_load_lds_dwordx4 v2, s[38:39] offset:1600
	global_load_lds_dwordx4 v2, s[40:41] offset:2624
	s_add_i32 m0, s26, 122304
	s_nop 0
	global_load_lds_dwordx4 v2, s[42:43] offset:576
	s_waitcnt vmcnt(21)
	s_barrier
	s_add_i32 m0, s26, 1408
	s_nop 0
	global_load_lds_dwordx4 v2, s[30:31] offset:640
	global_load_lds_dwordx4 v2, s[32:33] offset:1664
	global_load_lds_dwordx4 v2, s[34:35] offset:2688
	s_add_i32 m0, s26, 4480
	s_nop 0
	global_load_lds_dwordx4 v2, s[36:37] offset:640
	global_load_lds_dwordx4 v2, s[38:39] offset:1664
	global_load_lds_dwordx4 v2, s[40:41] offset:2688
	s_add_i32 m0, s26, 7552
	s_nop 0
	global_load_lds_dwordx4 v2, s[42:43] offset:640
	s_waitcnt vmcnt(21)
	s_barrier
	s_add_i32 m0, s26, 30016
	s_nop 0
	global_load_lds_dwordx4 v2, s[30:31] offset:704
	global_load_lds_dwordx4 v2, s[32:33] offset:1728
	global_load_lds_dwordx4 v2, s[34:35] offset:2752
	s_add_i32 m0, s26, 33088
	s_nop 0
	global_load_lds_dwordx4 v2, s[36:37] offset:704
	global_load_lds_dwordx4 v2, s[38:39] offset:1728
	global_load_lds_dwordx4 v2, s[40:41] offset:2752
	s_add_i32 m0, s26, 36160
	s_nop 0
	global_load_lds_dwordx4 v2, s[42:43] offset:704
	s_waitcnt vmcnt(21)
	s_barrier
	s_add_i32 m0, s26, 58624
	s_nop 0
	global_load_lds_dwordx4 v2, s[30:31] offset:768
	global_load_lds_dwordx4 v2, s[32:33] offset:1792
	global_load_lds_dwordx4 v2, s[34:35] offset:2816
	s_add_i32 m0, s26, 61696
	s_nop 0
	global_load_lds_dwordx4 v2, s[36:37] offset:768
	global_load_lds_dwordx4 v2, s[38:39] offset:1792
	global_load_lds_dwordx4 v2, s[40:41] offset:2816
	s_add_i32 m0, s26, 64768
	s_nop 0
	global_load_lds_dwordx4 v2, s[42:43] offset:768
	s_waitcnt vmcnt(21)
	s_barrier
	s_add_i32 m0, s26, 87232
	s_nop 0
	global_load_lds_dwordx4 v2, s[30:31] offset:832
	global_load_lds_dwordx4 v2, s[32:33] offset:1856
	global_load_lds_dwordx4 v2, s[34:35] offset:2880
	s_add_i32 m0, s26, 90304
	s_nop 0
	global_load_lds_dwordx4 v2, s[36:37] offset:832
	global_load_lds_dwordx4 v2, s[38:39] offset:1856
	global_load_lds_dwordx4 v2, s[40:41] offset:2880
	s_add_i32 m0, s26, 93376
	s_nop 0
	global_load_lds_dwordx4 v2, s[42:43] offset:832
	s_waitcnt vmcnt(21)
	s_barrier
	s_add_i32 m0, s26, 115840
	s_nop 0
	global_load_lds_dwordx4 v2, s[30:31] offset:896
	global_load_lds_dwordx4 v2, s[32:33] offset:1920
	global_load_lds_dwordx4 v2, s[34:35] offset:2944
	s_add_i32 m0, s26, 118912
	s_nop 0
	global_load_lds_dwordx4 v2, s[36:37] offset:896
	global_load_lds_dwordx4 v2, s[38:39] offset:1920
	global_load_lds_dwordx4 v2, s[40:41] offset:2944
	s_add_i32 m0, s26, 121984
	s_nop 0
	global_load_lds_dwordx4 v2, s[42:43] offset:896
	s_waitcnt vmcnt(21)
	s_barrier
	s_add_i32 m0, s26, 1088
	s_nop 0
	global_load_lds_dwordx4 v2, s[30:31] offset:960
	global_load_lds_dwordx4 v2, s[32:33] offset:1984
	global_load_lds_dwordx4 v2, s[34:35] offset:3008
	s_add_i32 m0, s26, 4160
	s_nop 0
	global_load_lds_dwordx4 v2, s[36:37] offset:960
	global_load_lds_dwordx4 v2, s[38:39] offset:1984
	global_load_lds_dwordx4 v2, s[40:41] offset:3008
	s_add_i32 m0, s26, 7232
	s_nop 0
	global_load_lds_dwordx4 v2, s[42:43] offset:960
	s_waitcnt vmcnt(21)
	s_barrier
	s_add_i32 m0, s26, 29696
	s_nop 0
	global_load_lds_dwordx4 v2, s[30:31] offset:1024
	global_load_lds_dwordx4 v2, s[32:33] offset:2048
	global_load_lds_dwordx4 v2, s[34:35] offset:3072
	s_add_i32 m0, s26, 32768
	s_nop 0
	global_load_lds_dwordx4 v2, s[36:37] offset:1024
	global_load_lds_dwordx4 v2, s[38:39] offset:2048
	global_load_lds_dwordx4 v2, s[40:41] offset:3072
	s_add_i32 m0, s26, 35840
	s_nop 0
	global_load_lds_dwordx4 v2, s[42:43] offset:1024
	s_waitcnt vmcnt(21)
	s_barrier
	s_add_i32 m0, s26, 58304
	s_nop 0
	global_load_lds_dwordx4 v2, s[30:31] offset:1088
	global_load_lds_dwordx4 v2, s[32:33] offset:2112
	global_load_lds_dwordx4 v2, s[34:35] offset:3136
	s_add_i32 m0, s26, 61376
	s_nop 0
	global_load_lds_dwordx4 v2, s[36:37] offset:1088
	global_load_lds_dwordx4 v2, s[38:39] offset:2112
	global_load_lds_dwordx4 v2, s[40:41] offset:3136
	s_add_i32 m0, s26, 64448
	s_nop 0
	global_load_lds_dwordx4 v2, s[42:43] offset:1088
	s_waitcnt vmcnt(21)
	s_barrier
	s_add_i32 m0, s26, 86912
	s_nop 0
	global_load_lds_dwordx4 v2, s[30:31] offset:1152
	global_load_lds_dwordx4 v2, s[32:33] offset:2176
	global_load_lds_dwordx4 v2, s[34:35] offset:3200
	s_add_i32 m0, s26, 89984
	s_nop 0
	global_load_lds_dwordx4 v2, s[36:37] offset:1152
	global_load_lds_dwordx4 v2, s[38:39] offset:2176
	global_load_lds_dwordx4 v2, s[40:41] offset:3200
	s_add_i32 m0, s26, 93056
	s_nop 0
	global_load_lds_dwordx4 v2, s[42:43] offset:1152
	s_waitcnt vmcnt(21)
	s_barrier
	s_add_i32 m0, s26, 115520
	s_nop 0
	global_load_lds_dwordx4 v2, s[30:31] offset:1216
	global_load_lds_dwordx4 v2, s[32:33] offset:2240
	global_load_lds_dwordx4 v2, s[34:35] offset:3264
	s_add_i32 m0, s26, 118592
	s_nop 0
	global_load_lds_dwordx4 v2, s[36:37] offset:1216
	global_load_lds_dwordx4 v2, s[38:39] offset:2240
	global_load_lds_dwordx4 v2, s[40:41] offset:3264
	s_add_i32 m0, s26, 121664
	s_nop 0
	global_load_lds_dwordx4 v2, s[42:43] offset:1216
	s_waitcnt vmcnt(21)
	s_barrier
	s_add_i32 m0, s26, 768
	s_nop 0
	global_load_lds_dwordx4 v2, s[30:31] offset:1280
	global_load_lds_dwordx4 v2, s[32:33] offset:2304
	global_load_lds_dwordx4 v2, s[34:35] offset:3328
	s_add_i32 m0, s26, 3840
	s_nop 0
	global_load_lds_dwordx4 v2, s[36:37] offset:1280
	global_load_lds_dwordx4 v2, s[38:39] offset:2304
	global_load_lds_dwordx4 v2, s[40:41] offset:3328
	s_add_i32 m0, s26, 6912
	s_nop 0
	global_load_lds_dwordx4 v2, s[42:43] offset:1280
	s_waitcnt vmcnt(21)
	s_barrier
	s_add_i32 m0, s26, 29376
	s_nop 0
	global_load_lds_dwordx4 v2, s[30:31] offset:1344
	global_load_lds_dwordx4 v2, s[32:33] offset:2368
	global_load_lds_dwordx4 v2, s[34:35] offset:3392
	s_add_i32 m0, s26, 32448
	s_nop 0
	global_load_lds_dwordx4 v2, s[36:37] offset:1344
	global_load_lds_dwordx4 v2, s[38:39] offset:2368
	global_load_lds_dwordx4 v2, s[40:41] offset:3392
	s_add_i32 m0, s26, 35520
	s_nop 0
	global_load_lds_dwordx4 v2, s[42:43] offset:1344
	s_waitcnt vmcnt(21)
	s_barrier
	s_add_i32 m0, s26, 57984
	s_nop 0
	global_load_lds_dwordx4 v2, s[30:31] offset:1408
	global_load_lds_dwordx4 v2, s[32:33] offset:2432
	global_load_lds_dwordx4 v2, s[34:35] offset:3456
	s_add_i32 m0, s26, 61056
	s_nop 0
	global_load_lds_dwordx4 v2, s[36:37] offset:1408
	global_load_lds_dwordx4 v2, s[38:39] offset:2432
	global_load_lds_dwordx4 v2, s[40:41] offset:3456
	s_add_i32 m0, s26, 64128
	s_nop 0
	global_load_lds_dwordx4 v2, s[42:43] offset:1408
	s_waitcnt vmcnt(21)
	s_barrier
	s_add_i32 m0, s26, 86592
	s_nop 0
	global_load_lds_dwordx4 v2, s[30:31] offset:1472
	global_load_lds_dwordx4 v2, s[32:33] offset:2496
	global_load_lds_dwordx4 v2, s[34:35] offset:3520
	s_add_i32 m0, s26, 89664
	s_nop 0
	global_load_lds_dwordx4 v2, s[36:37] offset:1472
	global_load_lds_dwordx4 v2, s[38:39] offset:2496
	global_load_lds_dwordx4 v2, s[40:41] offset:3520
	s_add_i32 m0, s26, 92736
	s_nop 0
	global_load_lds_dwordx4 v2, s[42:43] offset:1472
	s_waitcnt vmcnt(21)
	s_barrier
	s_waitcnt vmcnt(14)
	s_barrier
	s_waitcnt vmcnt(7)
	s_barrier
	s_waitcnt vmcnt(0)
	s_barrier

.LBB2_4:
	s_setprio 2
	s_load_dwordx4 s[4:7], s[0:1], 0x0
	s_add_i32 s13, s13, -4
	v_lshrrev_b32_e32 v1, 3, v1
	v_and_b32_e32 v30, 7, v0
	s_mul_i32 s10, s8, 0x600
	s_mul_i32 s11, s9, 0x600
	s_waitcnt lgkmcnt(0)
	s_add_u32 s4, s4, s10
	s_addc_u32 s5, s5, 0
	s_add_u32 s6, s6, s11
	s_addc_u32 s7, s7, 0
	s_cmp_eq_u32 s13, 1
	s_cselect_b32 s14, s6, s4
	s_cselect_b32 s15, s7, s5
	s_cselect_b32 s16, 0xffffa000, 0
	s_mul_i32 s17, s13, 0x2a000
	s_add_u32 s4, s4, s17
	s_addc_u32 s5, s5, 0
	s_ashr_i32 s17, s16, 31
	s_add_u32 s14, s14, s16
	s_addc_u32 s15, s15, s17
	v_and_b32_e32 v31, 63, v0
	v_lshrrev_b32_e32 v32, 4, v31
	v_xor_b32_e32 v32, v32, v30
	v_lshlrev_b32_e32 v32, 4, v32
	v_mul_u32_u24_e32 v2, 0x600, v1
	v_add_u32_e32 v2, v2, v32
	v_xor_b32_e32 v3, 64, v2
	s_add_u32 s20, s4, 0x0
	s_addc_u32 s21, s5, 0
	s_add_u32 s22, s4, 0x2c00
	s_addc_u32 s23, s5, 0
	s_add_u32 s24, s14, 0x5800
	s_addc_u32 s25, s15, 0
	s_add_u32 s26, s14, 0x9000
	s_addc_u32 s27, s15, 0
	s_add_u32 s28, s14, 0xbc00
	s_addc_u32 s29, s15, 0
	s_add_u32 s30, s14, 0xe800
	s_addc_u32 s31, s15, 0
	s_add_u32 s32, s14, 0x12000
	s_addc_u32 s33, s15, 0
	s_add_u32 s34, s14, 0x14c00
	s_addc_u32 s35, s15, 0
	s_add_u32 s36, s14, 0x17800
	s_addc_u32 s37, s15, 0
	s_add_u32 s38, s14, 0x1b000
	s_addc_u32 s39, s15, 0
	s_add_u32 s40, s14, 0x1dc00
	s_addc_u32 s41, s15, 0
	s_add_u32 s42, s14, 0x20800
	s_addc_u32 s43, s15, 0
	s_add_u32 s44, s14, 0x24000
	s_addc_u32 s45, s15, 0
	s_add_u32 s46, s14, 0x26c00
	s_addc_u32 s47, s15, 0
	s_mul_i32 s18, s13, 0x3800
	s_add_i32 m0, s18, 2048
	s_nop 0
	global_load_lds_dwordx4 v2, s[20:21]
	global_load_lds_dwordx4 v3, s[22:23] offset:1024
	global_load_lds_dwordx4 v2, s[24:25] offset:2048
	s_add_i32 m0, s18, 5120
	s_nop 0
	global_load_lds_dwordx4 v3, s[26:27]
	global_load_lds_dwordx4 v2, s[28:29] offset:1024
	global_load_lds_dwordx4 v3, s[30:31] offset:2048
	s_add_i32 m0, s18, 8192
	s_nop 0
	global_load_lds_dwordx4 v2, s[32:33]
	global_load_lds_dwordx4 v3, s[34:35] offset:1024
	global_load_lds_dwordx4 v2, s[36:37] offset:2048
	s_add_i32 m0, s18, 11264
	s_nop 0
	global_load_lds_dwordx4 v3, s[38:39]
	global_load_lds_dwordx4 v2, s[40:41] offset:1024
	global_load_lds_dwordx4 v3, s[42:43] offset:2048
	s_add_i32 m0, s18, 14336
	s_nop 0
	global_load_lds_dwordx4 v2, s[44:45]
	global_load_lds_dwordx4 v3, s[46:47] offset:1024
	s_add_i32 m0, s18, 30592
	s_nop 0
	global_load_lds_dwordx4 v2, s[20:21] offset:128
	global_load_lds_dwordx4 v3, s[22:23] offset:1152
	global_load_lds_dwordx4 v2, s[24:25] offset:2176
	s_add_i32 m0, s18, 33664
	s_nop 0
	global_load_lds_dwordx4 v3, s[26:27] offset:128
	global_load_lds_dwordx4 v2, s[28:29] offset:1152
	global_load_lds_dwordx4 v3, s[30:31] offset:2176
	s_add_i32 m0, s18, 36736
	s_nop 0
	global_load_lds_dwordx4 v2, s[32:33] offset:128
	global_load_lds_dwordx4 v3, s[34:35] offset:1152
	global_load_lds_dwordx4 v2, s[36:37] offset:2176
	s_add_i32 m0, s18, 39808
	s_nop 0
	global_load_lds_dwordx4 v3, s[38:39] offset:128
	global_load_lds_dwordx4 v2, s[40:41] offset:1152
	global_load_lds_dwordx4 v3, s[42:43] offset:2176
	s_add_i32 m0, s18, 42880
	s_nop 0
	global_load_lds_dwordx4 v2, s[44:45] offset:128
	global_load_lds_dwordx4 v3, s[46:47] offset:1152
	s_add_i32 m0, s18, 59136
	s_nop 0
	global_load_lds_dwordx4 v2, s[20:21] offset:256
	global_load_lds_dwordx4 v3, s[22:23] offset:1280
	global_load_lds_dwordx4 v2, s[24:25] offset:2304
	s_add_i32 m0, s18, 62208
	s_nop 0
	global_load_lds_dwordx4 v3, s[26:27] offset:256
	global_load_lds_dwordx4 v2, s[28:29] offset:1280
	global_load_lds_dwordx4 v3, s[30:31] offset:2304
	s_add_i32 m0, s18, 65280
	s_nop 0
	global_load_lds_dwordx4 v2, s[32:33] offset:256
	global_load_lds_dwordx4 v3, s[34:35] offset:1280
	global_load_lds_dwordx4 v2, s[36:37] offset:2304
	s_add_i32 m0, s18, 68352
	s_nop 0
	global_load_lds_dwordx4 v3, s[38:39] offset:256
	global_load_lds_dwordx4 v2, s[40:41] offset:1280
	global_load_lds_dwordx4 v3, s[42:43] offset:2304
	s_add_i32 m0, s18, 71424
	s_nop 0
	global_load_lds_dwordx4 v2, s[44:45] offset:256
	global_load_lds_dwordx4 v3, s[46:47] offset:1280
	s_add_i32 m0, s18, 87680
	s_nop 0
	global_load_lds_dwordx4 v2, s[20:21] offset:384
	global_load_lds_dwordx4 v3, s[22:23] offset:1408
	global_load_lds_dwordx4 v2, s[24:25] offset:2432
	s_add_i32 m0, s18, 90752
	s_nop 0
	global_load_lds_dwordx4 v3, s[26:27] offset:384
	global_load_lds_dwordx4 v2, s[28:29] offset:1408
	global_load_lds_dwordx4 v3, s[30:31] offset:2432
	s_add_i32 m0, s18, 93824
	s_nop 0
	global_load_lds_dwordx4 v2, s[32:33] offset:384
	global_load_lds_dwordx4 v3, s[34:35] offset:1408
	global_load_lds_dwordx4 v2, s[36:37] offset:2432
	s_add_i32 m0, s18, 96896
	s_nop 0
	global_load_lds_dwordx4 v3, s[38:39] offset:384
	global_load_lds_dwordx4 v2, s[40:41] offset:1408
	global_load_lds_dwordx4 v3, s[42:43] offset:2432
	s_add_i32 m0, s18, 99968
	s_nop 0
	global_load_lds_dwordx4 v2, s[44:45] offset:384
	global_load_lds_dwordx4 v3, s[46:47] offset:1408
	s_waitcnt vmcnt(42)
	s_barrier
	s_add_i32 m0, s18, 116224
	s_nop 0
	global_load_lds_dwordx4 v2, s[20:21] offset:512
	global_load_lds_dwordx4 v3, s[22:23] offset:1536
	global_load_lds_dwordx4 v2, s[24:25] offset:2560
	s_add_i32 m0, s18, 119296
	s_nop 0
	global_load_lds_dwordx4 v3, s[26:27] offset:512
	global_load_lds_dwordx4 v2, s[28:29] offset:1536
	global_load_lds_dwordx4 v3, s[30:31] offset:2560
	s_add_i32 m0, s18, 122368
	s_nop 0
	global_load_lds_dwordx4 v2, s[32:33] offset:512
	global_load_lds_dwordx4 v3, s[34:35] offset:1536
	global_load_lds_dwordx4 v2, s[36:37] offset:2560
	s_add_i32 m0, s18, 125440
	s_nop 0
	global_load_lds_dwordx4 v3, s[38:39] offset:512
	global_load_lds_dwordx4 v2, s[40:41] offset:1536
	global_load_lds_dwordx4 v3, s[42:43] offset:2560
	s_add_i32 m0, s18, 128512
	s_nop 0
	global_load_lds_dwordx4 v2, s[44:45] offset:512
	global_load_lds_dwordx4 v3, s[46:47] offset:1536
	s_waitcnt vmcnt(42)
	s_barrier
	s_add_i32 m0, s18, 1408
	s_nop 0
	global_load_lds_dwordx4 v2, s[20:21] offset:640
	global_load_lds_dwordx4 v3, s[22:23] offset:1664
	global_load_lds_dwordx4 v2, s[24:25] offset:2688
	s_add_i32 m0, s18, 4480
	s_nop 0
	global_load_lds_dwordx4 v3, s[26:27] offset:640
	global_load_lds_dwordx4 v2, s[28:29] offset:1664
	global_load_lds_dwordx4 v3, s[30:31] offset:2688
	s_add_i32 m0, s18, 7552
	s_nop 0
	global_load_lds_dwordx4 v2, s[32:33] offset:640
	global_load_lds_dwordx4 v3, s[34:35] offset:1664
	global_load_lds_dwordx4 v2, s[36:37] offset:2688
	s_add_i32 m0, s18, 10624
	s_nop 0
	global_load_lds_dwordx4 v3, s[38:39] offset:640
	global_load_lds_dwordx4 v2, s[40:41] offset:1664
	global_load_lds_dwordx4 v3, s[42:43] offset:2688
	s_add_i32 m0, s18, 13696
	s_nop 0
	global_load_lds_dwordx4 v2, s[44:45] offset:640
	global_load_lds_dwordx4 v3, s[46:47] offset:1664
	s_waitcnt vmcnt(42)
	s_barrier
	s_add_i32 m0, s18, 29952
	s_nop 0
	global_load_lds_dwordx4 v2, s[20:21] offset:768
	global_load_lds_dwordx4 v3, s[22:23] offset:1792
	global_load_lds_dwordx4 v2, s[24:25] offset:2816
	s_add_i32 m0, s18, 33024
	s_nop 0
	global_load_lds_dwordx4 v3, s[26:27] offset:768
	global_load_lds_dwordx4 v2, s[28:29] offset:1792
	global_load_lds_dwordx4 v3, s[30:31] offset:2816
	s_add_i32 m0, s18, 36096
	s_nop 0
	global_load_lds_dwordx4 v2, s[32:33] offset:768
	global_load_lds_dwordx4 v3, s[34:35] offset:1792
	global_load_lds_dwordx4 v2, s[36:37] offset:2816
	s_add_i32 m0, s18, 39168
	s_nop 0
	global_load_lds_dwordx4 v3, s[38:39] offset:768
	global_load_lds_dwordx4 v2, s[40:41] offset:1792
	global_load_lds_dwordx4 v3, s[42:43] offset:2816
	s_add_i32 m0, s18, 42240
	s_nop 0
	global_load_lds_dwordx4 v2, s[44:45] offset:768
	global_load_lds_dwordx4 v3, s[46:47] offset:1792
	s_waitcnt vmcnt(42)
	s_barrier
	s_add_i32 m0, s18, 58496
	s_nop 0
	global_load_lds_dwordx4 v2, s[20:21] offset:896
	global_load_lds_dwordx4 v3, s[22:23] offset:1920
	global_load_lds_dwordx4 v2, s[24:25] offset:2944
	s_add_i32 m0, s18, 61568
	s_nop 0
	global_load_lds_dwordx4 v3, s[26:27] offset:896
	global_load_lds_dwordx4 v2, s[28:29] offset:1920
	global_load_lds_dwordx4 v3, s[30:31] offset:2944
	s_add_i32 m0, s18, 64640
	s_nop 0
	global_load_lds_dwordx4 v2, s[32:33] offset:896
	global_load_lds_dwordx4 v3, s[34:35] offset:1920
	global_load_lds_dwordx4 v2, s[36:37] offset:2944
	s_add_i32 m0, s18, 67712
	s_nop 0
	global_load_lds_dwordx4 v3, s[38:39] offset:896
	global_load_lds_dwordx4 v2, s[40:41] offset:1920
	global_load_lds_dwordx4 v3, s[42:43] offset:2944
	s_add_i32 m0, s18, 70784
	s_nop 0
	global_load_lds_dwordx4 v2, s[44:45] offset:896
	global_load_lds_dwordx4 v3, s[46:47] offset:1920
	s_waitcnt vmcnt(42)
	s_barrier
	s_add_i32 m0, s18, 87040
	s_nop 0
	global_load_lds_dwordx4 v2, s[20:21] offset:1024
	global_load_lds_dwordx4 v3, s[22:23] offset:2048
	global_load_lds_dwordx4 v2, s[24:25] offset:3072
	s_add_i32 m0, s18, 90112
	s_nop 0
	global_load_lds_dwordx4 v3, s[26:27] offset:1024
	global_load_lds_dwordx4 v2, s[28:29] offset:2048
	global_load_lds_dwordx4 v3, s[30:31] offset:3072
	s_add_i32 m0, s18, 93184
	s_nop 0
	global_load_lds_dwordx4 v2, s[32:33] offset:1024
	global_load_lds_dwordx4 v3, s[34:35] offset:2048
	global_load_lds_dwordx4 v2, s[36:37] offset:3072
	s_add_i32 m0, s18, 96256
	s_nop 0
	global_load_lds_dwordx4 v3, s[38:39] offset:1024
	global_load_lds_dwordx4 v2, s[40:41] offset:2048
	global_load_lds_dwordx4 v3, s[42:43] offset:3072
	s_add_i32 m0, s18, 99328
	s_nop 0
	global_load_lds_dwordx4 v2, s[44:45] offset:1024
	global_load_lds_dwordx4 v3, s[46:47] offset:2048
	s_waitcnt vmcnt(42)
	s_barrier
	s_add_i32 m0, s18, 115584
	s_nop 0
	global_load_lds_dwordx4 v2, s[20:21] offset:1152
	global_load_lds_dwordx4 v3, s[22:23] offset:2176
	global_load_lds_dwordx4 v2, s[24:25] offset:3200
	s_add_i32 m0, s18, 118656
	s_nop 0
	global_load_lds_dwordx4 v3, s[26:27] offset:1152
	global_load_lds_dwordx4 v2, s[28:29] offset:2176
	global_load_lds_dwordx4 v3, s[30:31] offset:3200
	s_add_i32 m0, s18, 121728
	s_nop 0
	global_load_lds_dwordx4 v2, s[32:33] offset:1152
	global_load_lds_dwordx4 v3, s[34:35] offset:2176
	global_load_lds_dwordx4 v2, s[36:37] offset:3200
	s_add_i32 m0, s18, 124800
	s_nop 0
	global_load_lds_dwordx4 v3, s[38:39] offset:1152
	global_load_lds_dwordx4 v2, s[40:41] offset:2176
	global_load_lds_dwordx4 v3, s[42:43] offset:3200
	s_add_i32 m0, s18, 127872
	s_nop 0
	global_load_lds_dwordx4 v2, s[44:45] offset:1152
	global_load_lds_dwordx4 v3, s[46:47] offset:2176
	s_waitcnt vmcnt(42)
	s_barrier
	s_add_i32 m0, s18, 768
	s_nop 0
	global_load_lds_dwordx4 v2, s[20:21] offset:1280
	global_load_lds_dwordx4 v3, s[22:23] offset:2304
	global_load_lds_dwordx4 v2, s[24:25] offset:3328
	s_add_i32 m0, s18, 3840
	s_nop 0
	global_load_lds_dwordx4 v3, s[26:27] offset:1280
	global_load_lds_dwordx4 v2, s[28:29] offset:2304
	global_load_lds_dwordx4 v3, s[30:31] offset:3328
	s_add_i32 m0, s18, 6912
	s_nop 0
	global_load_lds_dwordx4 v2, s[32:33] offset:1280
	global_load_lds_dwordx4 v3, s[34:35] offset:2304
	global_load_lds_dwordx4 v2, s[36:37] offset:3328
	s_add_i32 m0, s18, 9984
	s_nop 0
	global_load_lds_dwordx4 v3, s[38:39] offset:1280
	global_load_lds_dwordx4 v2, s[40:41] offset:2304
	global_load_lds_dwordx4 v3, s[42:43] offset:3328
	s_add_i32 m0, s18, 13056
	s_nop 0
	global_load_lds_dwordx4 v2, s[44:45] offset:1280
	global_load_lds_dwordx4 v3, s[46:47] offset:2304
	s_waitcnt vmcnt(42)
	s_barrier
	s_add_i32 m0, s18, 29312
	s_nop 0
	global_load_lds_dwordx4 v2, s[20:21] offset:1408
	global_load_lds_dwordx4 v3, s[22:23] offset:2432
	global_load_lds_dwordx4 v2, s[24:25] offset:3456
	s_add_i32 m0, s18, 32384
	s_nop 0
	global_load_lds_dwordx4 v3, s[26:27] offset:1408
	global_load_lds_dwordx4 v2, s[28:29] offset:2432
	global_load_lds_dwordx4 v3, s[30:31] offset:3456
	s_add_i32 m0, s18, 35456
	s_nop 0
	global_load_lds_dwordx4 v2, s[32:33] offset:1408
	global_load_lds_dwordx4 v3, s[34:35] offset:2432
	global_load_lds_dwordx4 v2, s[36:37] offset:3456
	s_add_i32 m0, s18, 38528
	s_nop 0
	global_load_lds_dwordx4 v3, s[38:39] offset:1408
	global_load_lds_dwordx4 v2, s[40:41] offset:2432
	global_load_lds_dwordx4 v3, s[42:43] offset:3456
	s_add_i32 m0, s18, 41600
	s_nop 0
	global_load_lds_dwordx4 v2, s[44:45] offset:1408
	global_load_lds_dwordx4 v3, s[46:47] offset:2432
	s_waitcnt vmcnt(42)
	s_barrier
	s_waitcnt vmcnt(28)
	s_barrier
	s_waitcnt vmcnt(14)
	s_barrier
	s_waitcnt vmcnt(0)
	s_barrier
	s_endpgm
